# lever 4 (wave priority): in P2 a wave runs attention tasks at user priority 1 and conversion items at priority 0 (priority follows the role); reset at the P2->P3 seam
# speedup vs baseline: 1.0039x; 1.0039x over previous
.LBB0_436:
	s_xor_b64 s[6:7], s[88:89], -1
	s_and_b64 s[10:11], s[82:83], s[90:91]
	s_or_b64 s[6:7], s[6:7], s[10:11]
	s_mov_b64 s[0:1], -1
	s_and_b64 vcc, exec, s[6:7]
	s_cbranch_vccnz .LBB0_634
	s_setprio 0
	v_mov_b32_e32 v2, 0
	s_and_saveexec_b64 s[0:1], s[4:5]
	s_cbranch_execz .LBB0_441
	s_mov_b64 s[28:29], exec
	v_mbcnt_lo_u32_b32 v2, s28, 0
	v_mbcnt_hi_u32_b32 v2, s29, v2
	v_cmp_eq_u32_e32 vcc, 0, v2
	s_and_saveexec_b64 s[6:7], vcc
	s_cbranch_execz .LBB0_440
	s_bcnt1_i32_b64 s8, s[28:29]
	s_waitcnt vmcnt(22)
	v_mov_b32_e32 v4, s14
	v_mov_b32_e32 v5, s8
	ds_add_rtn_u32 v4, v4, v5

.LBB0_634:
	s_and_b64 vcc, exec, s[0:1]
	s_cbranch_vccz .LBB0_743
	s_setprio 1
	v_mov_b32_e32 v2, 0
	s_and_saveexec_b64 s[0:1], s[4:5]
	s_cbranch_execz .LBB0_639
	s_mov_b64 s[28:29], exec
	v_mbcnt_lo_u32_b32 v2, s28, 0
	v_mbcnt_hi_u32_b32 v2, s29, v2
	v_cmp_eq_u32_e32 vcc, 0, v2
	s_and_saveexec_b64 s[6:7], vcc
	s_cbranch_execz .LBB0_638
	s_bcnt1_i32_b64 s8, s[28:29]
	v_readlane_b32 s10, v255, 48
	s_waitcnt vmcnt(22)
	v_mov_b32_e32 v5, s8
	v_mov_b32_e32 v4, s10
	ds_add_rtn_u32 v4, v4, v5
